# NA work queue: next unit ticket requested one unit ahead (the atomic round trip at every unit start is no longer waited for)
# speedup vs baseline: 1.0083x; 1.0083x over previous
; #define LAS __attribute__((address_space(3)))
; __device__ __forceinline__ void na_fast_unit(int unit, const bf16_t* P, const float* rpb, bf16_t* AO, LAS unsigned char* lds) {
;     const int tid = threadIdx.x, lane = tid & 63, wv = __builtin_amdgcn_readfirstlane(tid >> 6);
;     const int cq = wv & 3, kh = wv >> 2;
;     const int r = unit & 63, h = (unit >> 6) & 7, b = unit >> 9;
;     const int l15 = lane & 15, q = lane >> 4, trq = l15 >> 2, trp = lane & 3;
;     const int rstart = min(max(r - 4, 0), 56);
;     const int col = 16 * cq + l15, cstart = min(max(col - 8, 0), 48);
;     const int ct0 = min(max(cq - 1, 0), 1);
;     const float scale = 0.08838834764831845f;
; __global__ void __launch_bounds__(512, 2) mk_fwd(Args a) {
;     ...
;         unsigned* qctr = (unsigned*)(ws + WS_CTL) + 8192 + 64 * rep;
;         for (;;) {
;             __syncthreads();
;             if (tid == 0) *(volatile LAS unsigned*)(lds + LDS_BARW + 32) = atomicAdd(qctr, 1u);
;             __syncthreads();
;             const unsigned u = *(volatile LAS unsigned*)(lds + LDS_BARW + 32);
;             if (u >= (unsigned)(NB * 8 * 64)) break;
;             na_fast_unit((int)u, Pb, a.in[I_RPB], AO, lds);
.LBB0_1206:
	v_or_b32_e32 v3, 0x600, v0
	s_add_u32 s8, s94, 0x8000
	v_and_b32_e32 v2, 0x78, v181
	v_or_b32_e32 v104, 64, v168
	v_lshrrev_b32_e32 v105, 4, v3
	v_readlane_b32 s6, v255, 3
	s_addc_u32 s9, s95, 0
	v_bfe_u32 v106, v3, 4, 6
	v_mul_u32_u24_e32 v107, 0x110, v168
	v_mul_u32_u24_e32 v108, 0x110, v170
	v_mul_u32_u24_e32 v109, 0x120, v104
	v_mul_u32_u24_e32 v110, 0x110, v105
	v_mul_u32_u24_e32 v111, 0x120, v105
	s_add_i32 s2, 0, 0x11800
	s_add_i32 s3, 0, 0x1a000
	v_lshlrev_b32_e32 v114, 11, v86
	v_lshl_add_u32 v115, v1, 2, 0
	v_lshlrev_b32_e32 v86, 1, v1
	v_readlane_b32 s7, v255, 4
	v_mov_b32_e32 v3, 0x200
	s_add_i32 s45, 0, 0x23fe0
	v_lshlrev_b32_e32 v92, 1, v2
	v_mbcnt_lo_u32_b32 v2, -1, 0
	v_cmp_eq_u32_e64 s[4:5], 0, v0
	s_movk_i32 s13, 0x110
	v_add_u32_e32 v112, s2, v176
	v_add_u32_e32 v113, s3, v178
	v_add_u32_e32 v116, v115, v114
	v_lshl_add_u64 v[88:89], s[6:7], 0, v[86:87]
	v_lshl_or_b32 v117, v169, 9, v3
	v_lshlrev_b32_e32 v118, 9, v180
	v_lshlrev_b32_e32 v119, 9, v179
	v_add_u32_e32 v120, 0, v176
	v_add_u32_e32 v121, 0, v178
	v_add_u32_e32 v122, s2, v177
	v_add_u32_e32 v123, s3, v177
	v_lshl_add_u32 v124, v169, 2, 0
	v_mov_b32_e32 v125, s45
	s_movk_i32 s46, 0x3200
	s_mov_b64 s[10:11], 0x1400
	s_movk_i32 s47, 0x1000
	v_add_u32_e32 v126, v174, v107
	v_add_u32_e32 v127, v174, v171
	v_add_u32_e32 v128, v174, v108
	v_add_u32_e32 v129, v174, v172
	v_add_u32_e32 v130, v174, v109
	v_add_u32_e32 v131, v174, v110
	v_add_u32_e32 v132, v174, v111
	s_mov_b32 s12, 0x3db504f3
	v_lshlrev_b32_e32 v90, 1, v175
	v_mbcnt_hi_u32_b32 v133, -1, v2
	s_and_saveexec_b64 s[2:3], s[4:5]
	v_mov_b32_e32 v3, 1
	global_atomic_add v253, v87, v3, s[8:9] sc0
	s_mov_b64 exec, s[2:3]
	s_branch .LBB0_1209

; #define LAS __attribute__((address_space(3)))
; __global__ void __launch_bounds__(512, 2) mk_fwd(Args a) {
;     ...
;         for (;;) {
;             __syncthreads();
;             if (tid == 0) *(volatile LAS unsigned*)(lds + LDS_BARW + 32) = atomicAdd(qctr, 1u);
;             __syncthreads();
;             const unsigned u = *(volatile LAS unsigned*)(lds + LDS_BARW + 32);
;             if (u >= (unsigned)(NB * 8 * 64)) break;
.LBB0_1209:
	s_waitcnt vmcnt(0) lgkmcnt(0)
	s_barrier
	s_and_saveexec_b64 s[2:3], s[4:5]
	s_cbranch_execz .LBB0_1213
	v_mov_b32_e32 v3, s45
	ds_write_b32 v3, v253
	v_mov_b32_e32 v2, 1
	s_nop 0
	global_atomic_add v253, v87, v2, s[8:9] sc0
